# P12 router/quantise loop: norm-weight vector staged once in LDS and read with ds_read_b128 instead of 8 global loads + vmcnt(0) per iteration (those also drained the next rows' prefetch)
# baseline (speedup 1.0000x reference)
.LBB0_912:
	s_or_b64 exec, exec, s[0:1]
	s_cmpk_lt_i32 s2, 0x100
	s_movk_i32 s33, 0x100
	s_cselect_b64 s[34:35], -1, 0
	s_cmpk_gt_i32 s2, 0xff
	v_cmp_eq_u32_e64 s[4:5], 0, v146
	v_or_b32_e32 v136, 64, v146
	v_lshlrev_b32_e32 v215, 4, v0
	v_add_u32_e32 v216, 0x2000, v215
	global_load_dwordx4 v[220:223], v216, s[52:53]
	v_add_u32_e32 v215, 0x1c000, v215
	s_waitcnt vmcnt(0)
	ds_write_b128 v215, v[220:223]
	s_waitcnt lgkmcnt(0)
	s_barrier
	s_cbranch_scc1 .LBB0_924
	v_mbcnt_lo_u32_b32 v1, -1, 0
	v_mbcnt_hi_u32_b32 v2, -1, v1
	v_and_b32_e32 v1, 64, v2
	v_add_u32_e32 v3, 64, v1
	v_and_b32_e32 v1, 1, v0
	v_cmp_eq_u32_e64 s[6:7], 0, v1
	v_xor_b32_e32 v1, 1, v2
	v_and_b32_e32 v4, 2, v0
	v_cmp_lt_i32_e32 vcc, v1, v3
	v_cmp_eq_u32_e64 s[8:9], 0, v4
	v_xor_b32_e32 v4, 2, v2
	v_cndmask_b32_e32 v1, v2, v1, vcc
	v_cmp_lt_i32_e32 vcc, v4, v3
	s_add_u32 s0, s52, 0x2000
	v_mov_b32_e32 v139, 0
	v_cndmask_b32_e32 v4, v2, v4, vcc
	v_lshlrev_b32_e32 v135, 2, v4
	v_and_b32_e32 v4, 4, v0
	v_cmp_eq_u32_e64 s[10:11], 0, v4
	v_xor_b32_e32 v4, 4, v2
	v_cmp_lt_i32_e32 vcc, v4, v3
	s_addc_u32 s1, s53, 0
	v_lshlrev_b32_e32 v14, 4, v136
	v_cndmask_b32_e32 v4, v2, v4, vcc
	v_lshlrev_b32_e32 v137, 2, v4
	v_and_b32_e32 v4, 8, v0
	v_cmp_eq_u32_e64 s[12:13], 0, v4
	v_xor_b32_e32 v4, 8, v2
	v_cmp_lt_i32_e32 vcc, v4, v3
	v_mov_b32_e32 v15, v139
	v_readlane_b32 s16, v242, 6
	v_cndmask_b32_e32 v4, v2, v4, vcc
	v_lshlrev_b32_e32 v147, 2, v4
	v_xor_b32_e32 v4, 16, v2
	v_cmp_lt_i32_e32 vcc, v4, v3
	v_lshl_add_u64 v[142:143], s[0:1], 0, v[14:15]
	s_lshl_b32 s44, s16, 3
	v_cndmask_b32_e32 v4, v2, v4, vcc
	v_lshlrev_b32_e32 v164, 2, v4
	v_xor_b32_e32 v4, 32, v2
	v_cmp_lt_i32_e32 vcc, v4, v3
	v_or_b32_e32 v6, 0x100, v146
	s_cmp_lt_u32 s96, 64
	v_cndmask_b32_e32 v2, v2, v4, vcc
	v_lshlrev_b32_e32 v165, 2, v2
	v_or_b32_e32 v2, 0x80, v146
	v_or_b32_e32 v4, 0xc0, v146
	v_lshlrev_b32_e32 v14, 4, v2
	v_lshl_add_u64 v[144:145], s[0:1], 0, v[14:15]
	v_lshlrev_b32_e32 v14, 4, v4
	v_or_b32_e32 v8, 0x140, v146
	v_lshl_add_u64 v[148:149], s[0:1], 0, v[14:15]
	v_lshlrev_b32_e32 v14, 4, v6
	s_cselect_b64 s[38:39], -1, 0
	s_add_i32 s3, 0, 0x10000
	v_or_b32_e32 v10, 0x180, v146
	v_lshl_add_u64 v[150:151], s[0:1], 0, v[14:15]
	v_lshlrev_b32_e32 v14, 4, v8
	v_lshlrev_b32_e32 v3, 2, v146
	v_or_b32_e32 v12, 0x1c0, v146
	v_lshl_add_u64 v[152:153], s[0:1], 0, v[14:15]
	v_lshlrev_b32_e32 v14, 4, v10
	s_add_u32 s45, s46, 0x20000
	v_add_u32_e32 v166, s3, v3
	v_lshlrev_b32_e32 v138, 4, v146
	v_add_u32_e32 v241, 0x1c000, v138
	v_lshl_add_u64 v[154:155], s[0:1], 0, v[14:15]
	v_lshlrev_b32_e32 v14, 4, v12
	s_addc_u32 s76, s47, 0
	s_ashr_i32 s3, s2, 31
	v_lshl_add_u64 v[140:141], s[0:1], 0, v[138:139]
	v_lshl_add_u64 v[156:157], s[0:1], 0, v[14:15]
	s_lshl_b64 s[0:1], s[2:3], 8
	s_lshl_b32 s14, s16, 5
	s_add_u32 s40, s0, s14
	s_addc_u32 s41, s1, 0
	s_ashr_i32 s89, s88, 31
	s_lshl_b64 s[42:43], s[88:89], 8
	s_add_i32 s77, s14, 0
	s_lshl_b64 s[0:1], s[2:3], 9
	s_and_b32 s14, s96, 0xffffffc0
	s_add_u32 s0, s0, s14
	s_addc_u32 s1, s1, 0
	s_add_u32 s48, s0, 0x410008
	v_readlane_b32 s17, v242, 7
	s_mov_b32 s36, 0
	s_addc_u32 s49, s1, 0
	s_lshl_b64 s[52:53], s[88:89], 9
	s_lshl_b64 s[0:1], s[2:3], 6
	s_mov_b32 s14, s16
	s_mov_b32 s17, s36
	s_add_u32 s54, s0, s44
	v_writelane_b32 v242, s14, 6
	s_addc_u32 s55, s1, 0
	s_lshl_b64 s[56:57], s[88:89], 6
	s_lshl_b64 s[0:1], s[2:3], 17
	v_writelane_b32 v242, s15, 7
	s_lshl_b64 s[14:15], s[16:17], 14
	s_add_u32 s0, s0, s14
	s_addc_u32 s1, s1, s15
	v_or_b32_e32 v14, s0, v3
	v_mov_b32_e32 v15, s1
	s_mov_b64 s[0:1], 0x1fe00800
	v_lshlrev_b32_e32 v1, 2, v1
	v_add_u32_e32 v167, 0, v138
	v_lshl_add_u64 v[158:159], v[14:15], 0, s[0:1]
	s_lshl_b64 s[58:59], s[88:89], 17
	v_lshlrev_b32_e32 v168, 4, v136
	v_lshlrev_b32_e32 v169, 4, v2
	v_lshlrev_b32_e32 v170, 4, v4
	v_lshlrev_b32_e32 v171, 4, v6
	v_lshlrev_b32_e32 v172, 4, v8
	v_lshlrev_b32_e32 v173, 4, v10
	v_lshlrev_b32_e32 v174, 4, v12
	v_mov_b32_e32 v175, 0x358637bd
	s_mov_b32 s3, 0xf800000
	v_mov_b32_e32 v176, 0x260
	s_mov_b32 s78, 0xc3e00000
	v_mov_b32_e32 v177, 0x400000
	v_lshlrev_b32_e32 v178, 4, v146
	v_mov_b32_e32 v179, 0x43e00000
	v_mov_b32_e32 v180, 0xff800000
	v_mov_b32_e32 v181, 1
	v_mov_b32_e32 v182, 2
	v_mov_b32_e32 v183, 3
	v_mov_b32_e32 v184, 4
	v_mov_b32_e32 v185, 5
	v_mov_b32_e32 v186, 6
	v_mov_b32_e32 v187, 7
	s_mov_b32 s60, s2
	s_branch .LBB0_916

.LBB0_918:
	s_waitcnt vmcnt(14)
	v_mov_b64_e32 v[116:117], v[20:21]
	v_mov_b64_e32 v[124:125], v[12:13]
	v_mov_b64_e32 v[114:115], v[18:19]
	v_mov_b64_e32 v[122:123], v[10:11]
	v_mov_b32_e32 v196, v125
	v_mov_b32_e32 v197, v117
	v_mov_b32_e32 v192, v123
	v_mov_b32_e32 v193, v115
	v_mov_b32_e32 v194, v124
	v_mov_b32_e32 v195, v116
	v_pk_mul_f32 v[196:197], v[196:197], v[196:197]
	s_waitcnt vmcnt(12)
	v_mov_b64_e32 v[120:121], v[16:17]
	v_mov_b64_e32 v[128:129], v[8:9]
	v_pk_mul_f32 v[192:193], v[192:193], v[192:193]
	v_pk_fma_f32 v[194:195], v[194:195], v[194:195], v[196:197]
	v_mov_b32_e32 v196, v122
	v_mov_b32_e32 v197, v114
	s_waitcnt vmcnt(11)
	v_mov_b64_e32 v[108:109], v[32:33]
	v_mov_b64_e32 v[118:119], v[14:15]
	v_mov_b64_e32 v[126:127], v[6:7]
	v_pk_fma_f32 v[192:193], v[196:197], v[196:197], v[192:193]
	v_mov_b32_e32 v198, v129
	v_mov_b32_e32 v199, v121
	s_waitcnt vmcnt(10)
	v_mov_b64_e32 v[100:101], v[40:41]
	v_mov_b64_e32 v[106:107], v[30:31]
	v_pk_add_f32 v[192:193], v[192:193], v[194:195]
	v_mov_b32_e32 v194, v127
	v_mov_b32_e32 v195, v119
	v_mov_b32_e32 v196, v128
	v_mov_b32_e32 v197, v120
	v_pk_mul_f32 v[198:199], v[198:199], v[198:199]
	v_mov_b64_e32 v[98:99], v[38:39]
	v_pk_mul_f32 v[6:7], v[108:109], v[108:109]
	v_pk_mul_f32 v[8:9], v[106:107], v[106:107]
	v_pk_mul_f32 v[194:195], v[194:195], v[194:195]
	v_pk_fma_f32 v[196:197], v[196:197], v[196:197], v[198:199]
	v_mov_b32_e32 v198, v126
	v_mov_b32_e32 v199, v118
	s_waitcnt vmcnt(7)
	v_mov_b64_e32 v[96:97], v[48:49]
	v_mov_b64_e32 v[112:113], v[24:25]
	v_pk_mov_b32 v[10:11], v[8:9], v[6:7] op_sel:[1,0]
	v_mov_b32_e32 v9, v7
	v_pk_fma_f32 v[194:195], v[198:199], v[198:199], v[194:195]
	v_mul_f32_e32 v138, v99, v99
	v_mov_b64_e32 v[94:95], v[46:47]
	v_mov_b64_e32 v[104:105], v[28:29]
	v_mov_b64_e32 v[110:111], v[22:23]
	v_pk_add_f32 v[130:131], v[10:11], v[8:9]
	v_pk_add_f32 v[194:195], v[194:195], v[196:197]
	v_pk_fma_f32 v[196:197], v[98:99], v[98:99], v[138:139] op_sel_hi:[1,1,0]
	v_mul_f32_e32 v138, v101, v101
	v_mov_b64_e32 v[102:103], v[26:27]
	v_pk_mul_f32 v[6:7], v[112:113], v[112:113]
	v_pk_mul_f32 v[8:9], v[110:111], v[110:111]
	v_mul_f32_e32 v162, v94, v94
	v_mul_f32_e32 v200, v95, v95
	v_mul_f32_e32 v201, v96, v96
	v_mul_f32_e32 v202, v97, v97
	v_pk_fma_f32 v[198:199], v[100:101], v[100:101], v[138:139] op_sel_hi:[1,1,0]
	v_pk_add_f32 v[192:193], v[192:193], v[192:193] op_sel:[0,1] op_sel_hi:[1,0]
	v_pk_add_f32 v[130:131], v[130:131], v[130:131] op_sel:[0,1] op_sel_hi:[1,0]
	s_waitcnt vmcnt(6)
	v_mov_b64_e32 v[92:93], v[36:37]
	v_pk_mov_b32 v[10:11], v[8:9], v[6:7] op_sel:[1,0]
	v_mov_b32_e32 v9, v7
	v_mov_b32_e32 v197, v201
	v_mov_b32_e32 v199, v202
	v_mov_b32_e32 v193, v162
	v_mov_b32_e32 v131, v200
	v_mul_f32_e32 v138, v103, v103
	s_waitcnt vmcnt(5)
	v_mov_b64_e32 v[84:85], v[56:57]
	v_mov_b64_e32 v[90:91], v[34:35]
	v_pk_add_f32 v[132:133], v[10:11], v[8:9]
	v_pk_add_f32 v[196:197], v[196:197], v[198:199]
	v_pk_add_f32 v[130:131], v[192:193], v[130:131]
	v_pk_fma_f32 v[192:193], v[102:103], v[102:103], v[138:139] op_sel_hi:[1,1,0]
	v_mul_f32_e32 v138, v105, v105
	s_waitcnt vmcnt(3)
	v_mov_b64_e32 v[76:77], v[64:65]
	v_mov_b64_e32 v[82:83], v[54:55]
	v_mul_f32_e32 v203, v90, v90
	v_mul_f32_e32 v204, v91, v91
	v_mul_f32_e32 v205, v92, v92
	v_mul_f32_e32 v206, v93, v93
	v_pk_add_f32 v[130:131], v[130:131], v[196:197]
	v_pk_fma_f32 v[196:197], v[104:105], v[104:105], v[138:139] op_sel_hi:[1,1,0]
	v_pk_add_f32 v[194:195], v[194:195], v[194:195] op_sel:[0,1] op_sel_hi:[1,0]
	v_pk_add_f32 v[132:133], v[132:133], v[132:133] op_sel:[0,1] op_sel_hi:[1,0]
	v_mov_b64_e32 v[74:75], v[62:63]
	v_pk_mul_f32 v[6:7], v[84:85], v[84:85]
	v_pk_mul_f32 v[8:9], v[82:83], v[82:83]
	v_mov_b32_e32 v193, v205
	v_mov_b32_e32 v197, v206
	v_mov_b32_e32 v195, v203
	v_mov_b32_e32 v133, v204
	v_mov_b64_e32 v[88:89], v[44:45]
	v_pk_mov_b32 v[10:11], v[8:9], v[6:7] op_sel:[1,0]
	v_mov_b32_e32 v9, v7
	s_waitcnt vmcnt(1)
	v_mov_b64_e32 v[72:73], v[4:5]
	v_pk_add_f32 v[192:193], v[192:193], v[196:197]
	v_pk_add_f32 v[132:133], v[194:195], v[132:133]
	v_mul_f32_e32 v138, v75, v75
	v_mov_b64_e32 v[80:81], v[52:53]
	v_mov_b64_e32 v[86:87], v[42:43]
	v_pk_add_f32 v[188:189], v[10:11], v[8:9]
	v_mov_b64_e32 v[70:71], v[2:3]
	v_pk_add_f32 v[132:133], v[132:133], v[192:193]
	v_pk_fma_f32 v[192:193], v[74:75], v[74:75], v[138:139] op_sel_hi:[1,1,0]
	v_mul_f32_e32 v138, v77, v77
	v_mov_b64_e32 v[78:79], v[50:51]
	v_pk_mul_f32 v[6:7], v[88:89], v[88:89]
	v_pk_mul_f32 v[8:9], v[86:87], v[86:87]
	v_mul_f32_e32 v207, v70, v70
	v_mul_f32_e32 v208, v71, v71
	v_mul_f32_e32 v209, v72, v72
	v_mul_f32_e32 v210, v73, v73
	v_pk_fma_f32 v[194:195], v[76:77], v[76:77], v[138:139] op_sel_hi:[1,1,0]
	v_pk_add_f32 v[130:131], v[130:131], v[130:131] op_sel:[0,1] op_sel_hi:[1,0]
	v_pk_add_f32 v[188:189], v[188:189], v[188:189] op_sel:[0,1] op_sel_hi:[1,0]
	s_waitcnt vmcnt(0)
	v_mov_b64_e32 v[68:69], v[60:61]
	v_pk_mov_b32 v[10:11], v[8:9], v[6:7] op_sel:[1,0]
	v_mov_b32_e32 v9, v7
	v_mov_b32_e32 v193, v209
	v_mov_b32_e32 v195, v210
	v_mov_b32_e32 v131, v207
	v_mov_b32_e32 v189, v208
	v_mul_f32_e32 v138, v79, v79
	v_mov_b64_e32 v[66:67], v[58:59]
	v_pk_add_f32 v[190:191], v[10:11], v[8:9]
	v_pk_add_f32 v[192:193], v[192:193], v[194:195]
	v_pk_add_f32 v[130:131], v[130:131], v[188:189]
	v_pk_fma_f32 v[188:189], v[78:79], v[78:79], v[138:139] op_sel_hi:[1,1,0]
	v_mul_f32_e32 v138, v81, v81
	v_mul_f32_e32 v211, v66, v66
	v_mul_f32_e32 v212, v67, v67
	v_mul_f32_e32 v213, v68, v68
	v_mul_f32_e32 v214, v69, v69
	v_pk_add_f32 v[130:131], v[130:131], v[192:193]
	v_pk_fma_f32 v[192:193], v[80:81], v[80:81], v[138:139] op_sel_hi:[1,1,0]
	v_pk_add_f32 v[132:133], v[132:133], v[132:133] op_sel:[0,1] op_sel_hi:[1,0]
	v_pk_add_f32 v[190:191], v[190:191], v[190:191] op_sel:[0,1] op_sel_hi:[1,0]
	v_mov_b32_e32 v189, v213
	v_mov_b32_e32 v193, v214
	v_mov_b32_e32 v133, v211
	v_mov_b32_e32 v191, v212
	v_pk_add_f32 v[188:189], v[188:189], v[192:193]
	v_pk_add_f32 v[132:133], v[132:133], v[190:191]
	v_add_f32_e32 v130, v130, v131
	v_pk_add_f32 v[132:133], v[132:133], v[188:189]
	s_cmp_eq_u32 s37, 24
	v_add_f32_e32 v131, v132, v133
	ds_bpermute_b32 v132, v1, v130
	s_cselect_b32 s0, 0, 2
	s_add_u32 s0, s0, s62
	s_addc_u32 s1, 0, s63
	s_lshl_b64 s[0:1], s[0:1], 13
	s_waitcnt lgkmcnt(0)
	v_add_f32_e32 v130, v130, v132
	ds_bpermute_b32 v132, v1, v131
	s_add_u32 s0, s28, s0
	s_addc_u32 s1, s29, s1
	s_add_u32 s14, s0, 0x2000
	s_addc_u32 s15, s1, 0
	s_waitcnt lgkmcnt(0)
	v_add_f32_e32 v131, v131, v132
	ds_bpermute_b32 v132, v135, v130
	global_load_dwordx4 v[10:13], v178, s[0:1]
	global_load_dwordx4 v[6:9], v178, s[14:15]
	global_load_dwordx4 v[18:21], v178, s[0:1] offset:1024
	global_load_dwordx4 v[14:17], v168, s[14:15]
	global_load_dwordx4 v[30:33], v178, s[0:1] offset:2048
	global_load_dwordx4 v[22:25], v169, s[14:15]
	global_load_dwordx4 v[38:41], v178, s[0:1] offset:3072
	global_load_dwordx4 v[26:29], v170, s[14:15]
	global_load_dwordx4 v[46:49], v171, s[0:1]
	global_load_dwordx4 v[34:37], v171, s[14:15]
	global_load_dwordx4 v[54:57], v172, s[0:1]
	global_load_dwordx4 v[42:45], v172, s[14:15]
	global_load_dwordx4 v[62:65], v173, s[0:1]
	global_load_dwordx4 v[50:53], v173, s[14:15]
	global_load_dwordx4 v[2:5], v174, s[0:1]
	global_load_dwordx4 v[58:61], v174, s[14:15]
	s_waitcnt lgkmcnt(0)
	v_add_f32_e32 v130, v130, v132
	ds_bpermute_b32 v132, v135, v131
	s_waitcnt lgkmcnt(0)
	v_add_f32_e32 v131, v131, v132
	ds_bpermute_b32 v132, v137, v130
	s_waitcnt lgkmcnt(0)
	v_add_f32_e32 v130, v130, v132
	ds_bpermute_b32 v132, v137, v131
	s_waitcnt lgkmcnt(0)
	v_add_f32_e32 v131, v131, v132
	ds_bpermute_b32 v132, v147, v130
	s_waitcnt lgkmcnt(0)
	v_add_f32_e32 v130, v130, v132
	ds_bpermute_b32 v132, v147, v131
	s_waitcnt lgkmcnt(0)
	v_add_f32_e32 v131, v131, v132
	ds_bpermute_b32 v132, v164, v130
	s_waitcnt lgkmcnt(0)
	v_add_f32_e32 v130, v130, v132
	ds_bpermute_b32 v132, v164, v131
	s_waitcnt lgkmcnt(0)
	v_add_f32_e32 v131, v131, v132
	ds_bpermute_b32 v132, v165, v130
	s_waitcnt lgkmcnt(0)
	v_add_f32_e32 v130, v130, v132
	ds_bpermute_b32 v132, v165, v131
	v_fmamk_f32 v130, v130, 0x3a000000, v175
	v_cmp_gt_f32_e32 vcc, s3, v130
	s_waitcnt lgkmcnt(0)
	v_add_f32_e32 v131, v131, v132
	v_mul_f32_e32 v132, 0x4f800000, v130
	v_cndmask_b32_e32 v130, v130, v132, vcc
	v_sqrt_f32_e32 v132, v130
	s_nop 0
	v_add_u32_e32 v133, -1, v132
	v_fma_f32 v138, -v133, v132, v130
	v_cmp_ge_f32_e64 s[0:1], 0, v138
	v_add_u32_e32 v138, 1, v132
	s_nop 0
	v_cndmask_b32_e64 v133, v132, v133, s[0:1]
	v_fma_f32 v132, -v138, v132, v130
	v_cmp_lt_f32_e64 s[0:1], 0, v132
	s_nop 1
	v_cndmask_b32_e64 v132, v133, v138, s[0:1]
	v_mul_f32_e32 v133, 0x37800000, v132
	v_cndmask_b32_e32 v132, v132, v133, vcc
	v_cmp_class_f32_e32 vcc, v130, v176
	s_nop 1
	v_cndmask_b32_e32 v130, v132, v130, vcc
	v_div_scale_f32 v132, s[0:1], v130, v130, 1.0
	v_rcp_f32_e32 v133, v132
	s_nop 0
	v_fma_f32 v138, -v132, v133, 1.0
	v_fmac_f32_e32 v133, v138, v133
	v_div_scale_f32 v138, vcc, 1.0, v130, 1.0
	v_mul_f32_e32 v162, v138, v133
	v_fma_f32 v188, -v132, v162, v138
	v_fmac_f32_e32 v162, v188, v133
	v_fma_f32 v132, -v132, v162, v138
	v_div_fmas_f32 v132, v132, v133, v162
	v_div_fixup_f32 v162, v132, v130, 1.0
	v_fmamk_f32 v130, v131, 0x3a000000, v175
	v_cmp_gt_f32_e32 vcc, s3, v130
	v_mul_f32_e32 v131, 0x4f800000, v130
	v_pk_mul_f32 v[122:123], v[122:123], v[162:163] op_sel_hi:[1,0]
	v_cndmask_b32_e32 v130, v130, v131, vcc
	v_sqrt_f32_e32 v131, v130
	v_pk_mul_f32 v[124:125], v[124:125], v[162:163] op_sel_hi:[1,0]
	v_pk_mul_f32 v[114:115], v[114:115], v[162:163] op_sel_hi:[1,0]
	v_pk_mul_f32 v[116:117], v[116:117], v[162:163] op_sel_hi:[1,0]
	v_add_u32_e32 v132, -1, v131
	v_fma_f32 v133, -v132, v131, v130
	v_cmp_ge_f32_e64 s[0:1], 0, v133
	v_add_u32_e32 v133, 1, v131
	v_pk_mul_f32 v[106:107], v[106:107], v[162:163] op_sel_hi:[1,0]
	v_cndmask_b32_e64 v132, v131, v132, s[0:1]
	v_fma_f32 v131, -v133, v131, v130
	v_cmp_lt_f32_e64 s[0:1], 0, v131
	v_pk_mul_f32 v[108:109], v[108:109], v[162:163] op_sel_hi:[1,0]
	v_pk_mul_f32 v[98:99], v[98:99], v[162:163] op_sel_hi:[1,0]
	v_cndmask_b32_e64 v131, v132, v133, s[0:1]
	v_mul_f32_e32 v132, 0x37800000, v131
	v_cndmask_b32_e32 v131, v131, v132, vcc
	v_cmp_class_f32_e32 vcc, v130, v176
	v_pk_mul_f32 v[100:101], v[100:101], v[162:163] op_sel_hi:[1,0]
	v_pk_mul_f32 v[82:83], v[82:83], v[162:163] op_sel_hi:[1,0]
	v_cndmask_b32_e32 v130, v131, v130, vcc
	v_div_scale_f32 v131, s[0:1], v130, v130, 1.0
	v_rcp_f32_e32 v132, v131
	v_pk_mul_f32 v[84:85], v[84:85], v[162:163] op_sel_hi:[1,0]
	v_pk_mul_f32 v[74:75], v[74:75], v[162:163] op_sel_hi:[1,0]
	v_pk_mul_f32 v[76:77], v[76:77], v[162:163] op_sel_hi:[1,0]
	v_fma_f32 v133, -v131, v132, 1.0
	v_fmac_f32_e32 v132, v133, v132
	v_div_scale_f32 v133, vcc, 1.0, v130, 1.0
	v_mul_f32_e32 v138, v133, v132
	v_fma_f32 v188, -v131, v138, v133
	v_fmac_f32_e32 v138, v188, v132
	v_fma_f32 v131, -v131, v138, v133
	v_div_fmas_f32 v131, v131, v132, v138
	v_div_fixup_f32 v138, v131, v130, 1.0
	ds_read_b128 v[130:133], v241
	v_pk_mul_f32 v[92:93], v[92:93], v[138:139] op_sel_hi:[1,0]
	v_pk_mul_f32 v[90:91], v[90:91], v[138:139] op_sel_hi:[1,0]
	v_pk_mul_f32 v[70:71], v[70:71], v[162:163] op_sel_hi:[1,0]
	v_pk_mul_f32 v[66:67], v[66:67], v[138:139] op_sel_hi:[1,0]
	v_pk_mul_f32 v[72:73], v[72:73], v[162:163] op_sel_hi:[1,0]
	v_pk_mul_f32 v[68:69], v[68:69], v[138:139] op_sel_hi:[1,0]
	s_waitcnt lgkmcnt(0)
	v_pk_mul_f32 v[190:191], v[130:131], v[122:123]
	v_pk_mul_f32 v[122:123], v[126:127], v[138:139] op_sel_hi:[1,0]
	v_mov_b32_e32 v126, 0
	v_pk_mul_f32 v[192:193], v[130:131], v[122:123]
	v_med3_f32 v122, v190, s78, v179
	v_med3_f32 v123, v191, s78, v179
	v_cvt_pk_fp8_f32 v126, v122, v123
	v_pk_mul_f32 v[188:189], v[132:133], v[124:125]
	v_pk_mul_f32 v[124:125], v[128:129], v[138:139] op_sel_hi:[1,0]
	v_mov_b32_e32 v128, 0
	v_pk_mul_f32 v[132:133], v[132:133], v[124:125]
	v_med3_f32 v124, v188, s78, v179
	v_med3_f32 v125, v189, s78, v179
	v_cvt_pk_fp8_f32 v126, v124, v125 op_sel:[0,0,1]
	v_med3_f32 v124, v192, s78, v179
	v_med3_f32 v125, v193, s78, v179
	v_cvt_pk_fp8_f32 v128, v124, v125
	v_lshl_add_u64 v[122:123], s[46:47], 0, v[160:161]
	global_store_dword v[122:123], v126, off offset:-2048
	v_med3_f32 v126, v132, s78, v179
	v_med3_f32 v127, v133, s78, v179
	v_cvt_pk_fp8_f32 v128, v126, v127 op_sel:[0,0,1]
	global_store_dword v[122:123], v128, off
	ds_read_b128 v[124:127], v167
	ds_read_b128 v[128:131], v167 offset:32768
	s_waitcnt lgkmcnt(1)
	v_pk_fma_f32 v[194:195], v[124:125], v[190:191], 0 op_sel_hi:[1,0,0]
	v_pk_fma_f32 v[196:197], v[126:127], v[190:191], 0 op_sel_hi:[1,0,0]
	s_waitcnt lgkmcnt(0)
	v_pk_fma_f32 v[198:199], v[190:191], v[128:129], 0 op_sel_hi:[0,1,0]
	v_pk_fma_f32 v[200:201], v[190:191], v[130:131], 0 op_sel_hi:[0,1,0]
	v_pk_fma_f32 v[202:203], v[124:125], v[192:193], 0 op_sel_hi:[1,0,0]
	v_pk_fma_f32 v[204:205], v[126:127], v[192:193], 0 op_sel_hi:[1,0,0]
	v_pk_fma_f32 v[206:207], v[128:129], v[192:193], 0 op_sel_hi:[1,0,0]
	v_pk_fma_f32 v[208:209], v[130:131], v[192:193], 0 op_sel_hi:[1,0,0]
	ds_read_b128 v[124:127], v167 offset:1024
	ds_read_b128 v[128:131], v167 offset:33792
	s_waitcnt lgkmcnt(1)
	v_pk_fma_f32 v[196:197], v[190:191], v[126:127], v[196:197] op_sel:[1,0,0]
	v_pk_fma_f32 v[194:195], v[190:191], v[124:125], v[194:195] op_sel:[1,0,0]
	s_waitcnt lgkmcnt(0)
	v_pk_fma_f32 v[200:201], v[190:191], v[130:131], v[200:201] op_sel:[1,0,0]
	v_pk_fma_f32 v[190:191], v[190:191], v[128:129], v[198:199] op_sel:[1,0,0]
	v_pk_fma_f32 v[198:199], v[192:193], v[126:127], v[204:205] op_sel:[1,0,0]
	v_pk_fma_f32 v[202:203], v[192:193], v[124:125], v[202:203] op_sel:[1,0,0]
	v_pk_fma_f32 v[204:205], v[192:193], v[130:131], v[208:209] op_sel:[1,0,0]
	v_pk_fma_f32 v[192:193], v[192:193], v[128:129], v[206:207] op_sel:[1,0,0]
	ds_read_b128 v[124:127], v167 offset:2048
	ds_read_b128 v[128:131], v167 offset:34816
	s_waitcnt lgkmcnt(1)
	v_pk_fma_f32 v[194:195], v[188:189], v[124:125], v[194:195] op_sel_hi:[0,1,1]
	v_pk_fma_f32 v[196:197], v[188:189], v[126:127], v[196:197] op_sel_hi:[0,1,1]
	s_waitcnt lgkmcnt(0)
	v_pk_fma_f32 v[190:191], v[188:189], v[128:129], v[190:191] op_sel_hi:[0,1,1]
	v_pk_fma_f32 v[200:201], v[188:189], v[130:131], v[200:201] op_sel_hi:[0,1,1]
	v_pk_fma_f32 v[202:203], v[132:133], v[124:125], v[202:203] op_sel_hi:[0,1,1]
	v_pk_fma_f32 v[198:199], v[132:133], v[126:127], v[198:199] op_sel_hi:[0,1,1]
	v_pk_fma_f32 v[192:193], v[132:133], v[128:129], v[192:193] op_sel_hi:[0,1,1]
	v_pk_fma_f32 v[204:205], v[132:133], v[130:131], v[204:205] op_sel_hi:[0,1,1]
	ds_read_b128 v[124:127], v167 offset:3072
	ds_read_b128 v[128:131], v167 offset:35840
	s_waitcnt lgkmcnt(1)
	v_pk_fma_f32 v[196:197], v[188:189], v[126:127], v[196:197] op_sel:[1,0,0]
	v_pk_fma_f32 v[194:195], v[188:189], v[124:125], v[194:195] op_sel:[1,0,0]
	s_waitcnt lgkmcnt(0)
	v_pk_fma_f32 v[200:201], v[188:189], v[130:131], v[200:201] op_sel:[1,0,0]
	v_pk_fma_f32 v[188:189], v[188:189], v[128:129], v[190:191] op_sel:[1,0,0]
	v_pk_fma_f32 v[190:191], v[132:133], v[126:127], v[198:199] op_sel:[1,0,0]
	v_pk_fma_f32 v[198:199], v[132:133], v[124:125], v[202:203] op_sel:[1,0,0]
	ds_read_b128 v[124:127], v241 offset:1024
	v_pk_fma_f32 v[128:129], v[132:133], v[128:129], v[192:193] op_sel:[1,0,0]
	v_pk_fma_f32 v[130:131], v[132:133], v[130:131], v[204:205] op_sel:[1,0,0]
	s_waitcnt lgkmcnt(0)
	v_pk_mul_f32 v[192:193], v[114:115], v[124:125]
	v_pk_mul_f32 v[114:115], v[118:119], v[138:139] op_sel_hi:[1,0]
	v_mov_b32_e32 v118, 0
	v_pk_mul_f32 v[124:125], v[114:115], v[124:125]
	v_med3_f32 v114, v192, s78, v179
	v_med3_f32 v115, v193, s78, v179
	v_cvt_pk_fp8_f32 v118, v114, v115
	v_pk_mul_f32 v[132:133], v[116:117], v[126:127]
	v_pk_mul_f32 v[116:117], v[120:121], v[138:139] op_sel_hi:[1,0]
	v_med3_f32 v114, v124, s78, v179
	v_pk_mul_f32 v[126:127], v[116:117], v[126:127]
	v_med3_f32 v116, v132, s78, v179
	v_med3_f32 v117, v133, s78, v179
	v_cvt_pk_fp8_f32 v118, v116, v117 op_sel:[0,0,1]
	v_med3_f32 v115, v125, s78, v179
	v_med3_f32 v116, v126, s78, v179
	v_med3_f32 v117, v127, s78, v179
	global_store_dword v[122:123], v118, off offset:-1792
	v_mov_b32_e32 v118, 0
	v_cvt_pk_fp8_f32 v118, v114, v115
	v_cvt_pk_fp8_f32 v118, v116, v117 op_sel:[0,0,1]
	global_store_dword v[122:123], v118, off offset:256
	ds_read_b128 v[114:117], v167 offset:4096
	ds_read_b128 v[118:121], v167 offset:36864
	s_waitcnt lgkmcnt(1)
	v_pk_fma_f32 v[194:195], v[192:193], v[114:115], v[194:195] op_sel_hi:[0,1,1]
	v_pk_fma_f32 v[196:197], v[192:193], v[116:117], v[196:197] op_sel_hi:[0,1,1]
	s_waitcnt lgkmcnt(0)
	v_pk_fma_f32 v[188:189], v[192:193], v[118:119], v[188:189] op_sel_hi:[0,1,1]
	v_pk_fma_f32 v[200:201], v[192:193], v[120:121], v[200:201] op_sel_hi:[0,1,1]
	v_pk_fma_f32 v[198:199], v[124:125], v[114:115], v[198:199] op_sel_hi:[0,1,1]
	v_pk_fma_f32 v[190:191], v[124:125], v[116:117], v[190:191] op_sel_hi:[0,1,1]
	v_pk_fma_f32 v[128:129], v[124:125], v[118:119], v[128:129] op_sel_hi:[0,1,1]
	v_pk_fma_f32 v[130:131], v[124:125], v[120:121], v[130:131] op_sel_hi:[0,1,1]
	ds_read_b128 v[114:117], v167 offset:5120
	ds_read_b128 v[118:121], v167 offset:37888
	s_waitcnt lgkmcnt(1)
	v_pk_fma_f32 v[196:197], v[192:193], v[116:117], v[196:197] op_sel:[1,0,0]
	v_pk_fma_f32 v[194:195], v[192:193], v[114:115], v[194:195] op_sel:[1,0,0]
	s_waitcnt lgkmcnt(0)
	v_pk_fma_f32 v[200:201], v[192:193], v[120:121], v[200:201] op_sel:[1,0,0]
	v_pk_fma_f32 v[188:189], v[192:193], v[118:119], v[188:189] op_sel:[1,0,0]
	v_pk_fma_f32 v[190:191], v[124:125], v[116:117], v[190:191] op_sel:[1,0,0]
	v_pk_fma_f32 v[192:193], v[124:125], v[114:115], v[198:199] op_sel:[1,0,0]
	v_pk_fma_f32 v[130:131], v[124:125], v[120:121], v[130:131] op_sel:[1,0,0]
	v_pk_fma_f32 v[124:125], v[124:125], v[118:119], v[128:129] op_sel:[1,0,0]
	ds_read_b128 v[114:117], v167 offset:6144
	ds_read_b128 v[118:121], v167 offset:38912
	s_waitcnt lgkmcnt(1)
	v_pk_fma_f32 v[128:129], v[132:133], v[114:115], v[194:195] op_sel_hi:[0,1,1]
	v_pk_fma_f32 v[194:195], v[132:133], v[116:117], v[196:197] op_sel_hi:[0,1,1]
	s_waitcnt lgkmcnt(0)
	v_pk_fma_f32 v[188:189], v[132:133], v[118:119], v[188:189] op_sel_hi:[0,1,1]
	v_pk_fma_f32 v[196:197], v[132:133], v[120:121], v[200:201] op_sel_hi:[0,1,1]
	v_pk_fma_f32 v[192:193], v[126:127], v[114:115], v[192:193] op_sel_hi:[0,1,1]
	v_pk_fma_f32 v[190:191], v[126:127], v[116:117], v[190:191] op_sel_hi:[0,1,1]
	v_pk_fma_f32 v[124:125], v[126:127], v[118:119], v[124:125] op_sel_hi:[0,1,1]
	v_pk_fma_f32 v[130:131], v[126:127], v[120:121], v[130:131] op_sel_hi:[0,1,1]
	ds_read_b128 v[114:117], v167 offset:7168
	ds_read_b128 v[118:121], v167 offset:39936
	s_waitcnt lgkmcnt(1)
	v_pk_fma_f32 v[194:195], v[132:133], v[116:117], v[194:195] op_sel:[1,0,0]
	v_pk_fma_f32 v[128:129], v[132:133], v[114:115], v[128:129] op_sel:[1,0,0]
	s_waitcnt lgkmcnt(0)
	v_pk_fma_f32 v[196:197], v[132:133], v[120:121], v[196:197] op_sel:[1,0,0]
	v_pk_fma_f32 v[132:133], v[132:133], v[118:119], v[188:189] op_sel:[1,0,0]
	v_pk_fma_f32 v[188:189], v[126:127], v[116:117], v[190:191] op_sel:[1,0,0]
	v_pk_fma_f32 v[190:191], v[126:127], v[114:115], v[192:193] op_sel:[1,0,0]
	ds_read_b128 v[114:117], v241 offset:2048
	v_pk_fma_f32 v[118:119], v[126:127], v[118:119], v[124:125] op_sel:[1,0,0]
	v_pk_fma_f32 v[120:121], v[126:127], v[120:121], v[130:131] op_sel:[1,0,0]
	s_waitcnt lgkmcnt(0)
	v_pk_mul_f32 v[124:125], v[106:107], v[114:115]
	v_pk_mul_f32 v[106:107], v[110:111], v[138:139] op_sel_hi:[1,0]
	v_mov_b32_e32 v110, 0
	v_pk_mul_f32 v[114:115], v[106:107], v[114:115]
	v_med3_f32 v106, v124, s78, v179
	v_med3_f32 v107, v125, s78, v179
	v_cvt_pk_fp8_f32 v110, v106, v107
	v_pk_mul_f32 v[130:131], v[108:109], v[116:117]
	v_pk_mul_f32 v[108:109], v[112:113], v[138:139] op_sel_hi:[1,0]
	v_med3_f32 v106, v114, s78, v179
	v_pk_mul_f32 v[192:193], v[108:109], v[116:117]
	v_med3_f32 v108, v130, s78, v179
	v_med3_f32 v109, v131, s78, v179
	v_cvt_pk_fp8_f32 v110, v108, v109 op_sel:[0,0,1]
	v_med3_f32 v107, v115, s78, v179
	v_med3_f32 v108, v192, s78, v179
	v_med3_f32 v109, v193, s78, v179
	global_store_dword v[122:123], v110, off offset:-1536
	v_mov_b32_e32 v110, 0
	v_cvt_pk_fp8_f32 v110, v106, v107
	v_cvt_pk_fp8_f32 v110, v108, v109 op_sel:[0,0,1]
	global_store_dword v[122:123], v110, off offset:512
	ds_read_b128 v[106:109], v167 offset:8192
	ds_read_b128 v[110:113], v167 offset:40960
	s_waitcnt lgkmcnt(1)
	v_pk_fma_f32 v[116:117], v[124:125], v[106:107], v[128:129] op_sel_hi:[0,1,1]
	v_pk_fma_f32 v[126:127], v[124:125], v[108:109], v[194:195] op_sel_hi:[0,1,1]
	s_waitcnt lgkmcnt(0)
	v_pk_fma_f32 v[128:129], v[124:125], v[110:111], v[132:133] op_sel_hi:[0,1,1]
	v_pk_fma_f32 v[132:133], v[124:125], v[112:113], v[196:197] op_sel_hi:[0,1,1]
	v_pk_fma_f32 v[190:191], v[114:115], v[106:107], v[190:191] op_sel_hi:[0,1,1]
	v_pk_fma_f32 v[188:189], v[114:115], v[108:109], v[188:189] op_sel_hi:[0,1,1]
	v_pk_fma_f32 v[118:119], v[114:115], v[110:111], v[118:119] op_sel_hi:[0,1,1]
	v_pk_fma_f32 v[120:121], v[114:115], v[112:113], v[120:121] op_sel_hi:[0,1,1]
	ds_read_b128 v[106:109], v167 offset:9216
	ds_read_b128 v[110:113], v167 offset:41984
	s_waitcnt lgkmcnt(1)
	v_pk_fma_f32 v[126:127], v[124:125], v[108:109], v[126:127] op_sel:[1,0,0]
	v_pk_fma_f32 v[116:117], v[124:125], v[106:107], v[116:117] op_sel:[1,0,0]
	s_waitcnt lgkmcnt(0)
	v_pk_fma_f32 v[132:133], v[124:125], v[112:113], v[132:133] op_sel:[1,0,0]
	v_pk_fma_f32 v[124:125], v[124:125], v[110:111], v[128:129] op_sel:[1,0,0]
	v_pk_fma_f32 v[128:129], v[114:115], v[108:109], v[188:189] op_sel:[1,0,0]
	v_pk_fma_f32 v[188:189], v[114:115], v[106:107], v[190:191] op_sel:[1,0,0]
	v_pk_fma_f32 v[120:121], v[114:115], v[112:113], v[120:121] op_sel:[1,0,0]
	v_pk_fma_f32 v[114:115], v[114:115], v[110:111], v[118:119] op_sel:[1,0,0]
	ds_read_b128 v[106:109], v167 offset:10240
	ds_read_b128 v[110:113], v167 offset:43008
	s_waitcnt lgkmcnt(1)
	v_pk_fma_f32 v[190:191], v[130:131], v[108:109], v[126:127] op_sel_hi:[0,1,1]
	s_waitcnt lgkmcnt(0)
	v_pk_fma_f32 v[194:195], v[130:131], v[110:111], v[124:125] op_sel_hi:[0,1,1]
	v_pk_fma_f32 v[132:133], v[130:131], v[112:113], v[132:133] op_sel_hi:[0,1,1]
	v_pk_fma_f32 v[112:113], v[192:193], v[112:113], v[120:121] op_sel_hi:[0,1,1]
	ds_read_b128 v[118:121], v167 offset:11264
	ds_read_b128 v[124:127], v167 offset:44032
	v_pk_fma_f32 v[116:117], v[130:131], v[106:107], v[116:117] op_sel_hi:[0,1,1]
	v_pk_fma_f32 v[128:129], v[192:193], v[108:109], v[128:129] op_sel_hi:[0,1,1]
	v_pk_fma_f32 v[196:197], v[192:193], v[110:111], v[114:115] op_sel_hi:[0,1,1]
	v_pk_fma_f32 v[188:189], v[192:193], v[106:107], v[188:189] op_sel_hi:[0,1,1]
	s_waitcnt lgkmcnt(1)
	v_pk_fma_f32 v[106:107], v[130:131], v[120:121], v[190:191] op_sel:[1,0,0]
	v_pk_fma_f32 v[114:115], v[130:131], v[118:119], v[116:117] op_sel:[1,0,0]
	s_waitcnt lgkmcnt(0)
	v_pk_fma_f32 v[108:109], v[130:131], v[126:127], v[132:133] op_sel:[1,0,0]
	v_pk_fma_f32 v[116:117], v[130:131], v[124:125], v[194:195] op_sel:[1,0,0]
	v_pk_fma_f32 v[110:111], v[192:193], v[120:121], v[128:129] op_sel:[1,0,0]
	v_pk_fma_f32 v[112:113], v[192:193], v[126:127], v[112:113] op_sel:[1,0,0]
	v_pk_fma_f32 v[120:121], v[192:193], v[124:125], v[196:197] op_sel:[1,0,0]
	ds_read_b128 v[124:127], v241 offset:3072
	v_pk_fma_f32 v[118:119], v[192:193], v[118:119], v[188:189] op_sel:[1,0,0]
	s_waitcnt lgkmcnt(0)
	v_pk_mul_f32 v[130:131], v[98:99], v[124:125]
	v_pk_mul_f32 v[98:99], v[102:103], v[138:139] op_sel_hi:[1,0]
	v_mov_b32_e32 v102, 0
	v_pk_mul_f32 v[124:125], v[98:99], v[124:125]
	v_med3_f32 v98, v130, s78, v179
	v_med3_f32 v99, v131, s78, v179
	v_cvt_pk_fp8_f32 v102, v98, v99
	v_pk_mul_f32 v[128:129], v[100:101], v[126:127]
	v_pk_mul_f32 v[100:101], v[104:105], v[138:139] op_sel_hi:[1,0]
	v_med3_f32 v98, v124, s78, v179
	v_pk_mul_f32 v[126:127], v[100:101], v[126:127]
	v_med3_f32 v100, v128, s78, v179
	v_med3_f32 v101, v129, s78, v179
	v_cvt_pk_fp8_f32 v102, v100, v101 op_sel:[0,0,1]
	v_med3_f32 v99, v125, s78, v179
	v_med3_f32 v100, v126, s78, v179
	v_med3_f32 v101, v127, s78, v179
	global_store_dword v[122:123], v102, off offset:-1280
	v_mov_b32_e32 v102, 0
	v_cvt_pk_fp8_f32 v102, v98, v99
	v_cvt_pk_fp8_f32 v102, v100, v101 op_sel:[0,0,1]
	global_store_dword v[122:123], v102, off offset:768
	ds_read_b128 v[98:101], v167 offset:12288
	ds_read_b128 v[102:105], v167 offset:45056
	s_waitcnt lgkmcnt(1)
	v_pk_fma_f32 v[114:115], v[130:131], v[98:99], v[114:115] op_sel_hi:[0,1,1]
	v_pk_fma_f32 v[106:107], v[130:131], v[100:101], v[106:107] op_sel_hi:[0,1,1]
	s_waitcnt lgkmcnt(0)
	v_pk_fma_f32 v[116:117], v[130:131], v[102:103], v[116:117] op_sel_hi:[0,1,1]
	v_pk_fma_f32 v[108:109], v[130:131], v[104:105], v[108:109] op_sel_hi:[0,1,1]
	v_pk_fma_f32 v[118:119], v[124:125], v[98:99], v[118:119] op_sel_hi:[0,1,1]
	v_pk_fma_f32 v[110:111], v[124:125], v[100:101], v[110:111] op_sel_hi:[0,1,1]
	v_pk_fma_f32 v[120:121], v[124:125], v[102:103], v[120:121] op_sel_hi:[0,1,1]
	v_pk_fma_f32 v[112:113], v[124:125], v[104:105], v[112:113] op_sel_hi:[0,1,1]
	ds_read_b128 v[98:101], v167 offset:13312
	ds_read_b128 v[102:105], v167 offset:46080
	s_waitcnt lgkmcnt(1)
	v_pk_fma_f32 v[106:107], v[130:131], v[100:101], v[106:107] op_sel:[1,0,0]
	v_pk_fma_f32 v[114:115], v[130:131], v[98:99], v[114:115] op_sel:[1,0,0]
	s_waitcnt lgkmcnt(0)
	v_pk_fma_f32 v[108:109], v[130:131], v[104:105], v[108:109] op_sel:[1,0,0]
	v_pk_fma_f32 v[116:117], v[130:131], v[102:103], v[116:117] op_sel:[1,0,0]
	v_pk_fma_f32 v[110:111], v[124:125], v[100:101], v[110:111] op_sel:[1,0,0]
	v_pk_fma_f32 v[118:119], v[124:125], v[98:99], v[118:119] op_sel:[1,0,0]
	v_pk_fma_f32 v[112:113], v[124:125], v[104:105], v[112:113] op_sel:[1,0,0]
	v_pk_fma_f32 v[120:121], v[124:125], v[102:103], v[120:121] op_sel:[1,0,0]
	ds_read_b128 v[98:101], v167 offset:14336
	ds_read_b128 v[102:105], v167 offset:47104
	s_waitcnt lgkmcnt(1)
	v_pk_fma_f32 v[124:125], v[128:129], v[98:99], v[114:115] op_sel_hi:[0,1,1]
	s_waitcnt lgkmcnt(0)
	v_pk_fma_f32 v[130:131], v[128:129], v[102:103], v[116:117] op_sel_hi:[0,1,1]
	v_pk_fma_f32 v[108:109], v[128:129], v[104:105], v[108:109] op_sel_hi:[0,1,1]
	v_pk_fma_f32 v[132:133], v[126:127], v[100:101], v[110:111] op_sel_hi:[0,1,1]
	v_pk_fma_f32 v[104:105], v[126:127], v[104:105], v[112:113] op_sel_hi:[0,1,1]
	ds_read_b128 v[110:113], v167 offset:15360
	ds_read_b128 v[114:117], v167 offset:48128
	v_pk_fma_f32 v[106:107], v[128:129], v[100:101], v[106:107] op_sel_hi:[0,1,1]
	v_pk_fma_f32 v[118:119], v[126:127], v[98:99], v[118:119] op_sel_hi:[0,1,1]
	v_pk_fma_f32 v[120:121], v[126:127], v[102:103], v[120:121] op_sel_hi:[0,1,1]
	s_waitcnt lgkmcnt(1)
	v_pk_fma_f32 v[98:99], v[128:129], v[112:113], v[106:107] op_sel:[1,0,0]
	v_pk_fma_f32 v[106:107], v[128:129], v[110:111], v[124:125] op_sel:[1,0,0]
	s_waitcnt lgkmcnt(0)
	v_pk_fma_f32 v[100:101], v[128:129], v[116:117], v[108:109] op_sel:[1,0,0]
	v_pk_fma_f32 v[110:111], v[126:127], v[110:111], v[118:119] op_sel:[1,0,0]
	v_pk_fma_f32 v[104:105], v[126:127], v[116:117], v[104:105] op_sel:[1,0,0]
	ds_read_b128 v[116:119], v241 offset:4096
	v_pk_fma_f32 v[108:109], v[128:129], v[114:115], v[130:131] op_sel:[1,0,0]
	v_pk_fma_f32 v[102:103], v[126:127], v[112:113], v[132:133] op_sel:[1,0,0]
	v_pk_fma_f32 v[112:113], v[126:127], v[114:115], v[120:121] op_sel:[1,0,0]
	v_pk_mul_f32 v[114:115], v[94:95], v[162:163] op_sel_hi:[1,0]
	v_pk_mul_f32 v[94:95], v[96:97], v[162:163] op_sel_hi:[1,0]
	s_waitcnt lgkmcnt(0)
	v_pk_mul_f32 v[96:97], v[114:115], v[116:117]
	v_pk_mul_f32 v[94:95], v[94:95], v[118:119]
	v_pk_mul_f32 v[114:115], v[92:93], v[118:119]
	v_med3_f32 v92, v96, s78, v179
	v_med3_f32 v93, v97, s78, v179
	v_mov_b32_e32 v118, 0
	v_cvt_pk_fp8_f32 v118, v92, v93
	v_pk_mul_f32 v[90:91], v[90:91], v[116:117]
	v_med3_f32 v116, v94, s78, v179
	v_med3_f32 v117, v95, s78, v179
	v_cvt_pk_fp8_f32 v118, v116, v117 op_sel:[0,0,1]
	v_med3_f32 v92, v90, s78, v179
	v_med3_f32 v93, v91, s78, v179
	v_med3_f32 v116, v114, s78, v179
	global_store_dword v[122:123], v118, off offset:-1024
	v_mov_b32_e32 v118, 0
	v_cvt_pk_fp8_f32 v118, v92, v93
	v_med3_f32 v117, v115, s78, v179
	v_cvt_pk_fp8_f32 v118, v116, v117 op_sel:[0,0,1]
	global_store_dword v[122:123], v118, off offset:1024
	ds_read_b128 v[116:119], v167 offset:16384
	ds_read_b128 v[124:127], v167 offset:49152
	s_waitcnt lgkmcnt(1)
	v_pk_fma_f32 v[92:93], v[96:97], v[116:117], v[106:107] op_sel_hi:[0,1,1]
	v_pk_fma_f32 v[106:107], v[96:97], v[118:119], v[98:99] op_sel_hi:[0,1,1]
	s_waitcnt lgkmcnt(0)
	v_pk_fma_f32 v[120:121], v[96:97], v[126:127], v[100:101] op_sel_hi:[0,1,1]
	v_pk_fma_f32 v[110:111], v[90:91], v[116:117], v[110:111] op_sel_hi:[0,1,1]
	v_pk_fma_f32 v[116:117], v[90:91], v[118:119], v[102:103] op_sel_hi:[0,1,1]
	v_pk_fma_f32 v[118:119], v[90:91], v[126:127], v[104:105] op_sel_hi:[0,1,1]
	ds_read_b128 v[98:101], v167 offset:17408
	ds_read_b128 v[102:105], v167 offset:50176
	v_pk_fma_f32 v[108:109], v[96:97], v[124:125], v[108:109] op_sel_hi:[0,1,1]
	v_pk_fma_f32 v[112:113], v[90:91], v[124:125], v[112:113] op_sel_hi:[0,1,1]
	s_waitcnt lgkmcnt(1)
	v_pk_fma_f32 v[106:107], v[96:97], v[100:101], v[106:107] op_sel:[1,0,0]
	v_pk_fma_f32 v[124:125], v[96:97], v[98:99], v[92:93] op_sel:[1,0,0]
	s_waitcnt lgkmcnt(0)
	v_pk_fma_f32 v[120:121], v[96:97], v[104:105], v[120:121] op_sel:[1,0,0]
	v_pk_fma_f32 v[108:109], v[96:97], v[102:103], v[108:109] op_sel:[1,0,0]
	v_pk_fma_f32 v[100:101], v[90:91], v[100:101], v[116:117] op_sel:[1,0,0]
	v_pk_fma_f32 v[110:111], v[90:91], v[98:99], v[110:111] op_sel:[1,0,0]
	v_pk_fma_f32 v[104:105], v[90:91], v[104:105], v[118:119] op_sel:[1,0,0]
	v_pk_fma_f32 v[102:103], v[90:91], v[102:103], v[112:113] op_sel:[1,0,0]
	ds_read_b128 v[90:93], v167 offset:18432
	ds_read_b128 v[96:99], v167 offset:51200
	s_waitcnt lgkmcnt(1)
	v_pk_fma_f32 v[116:117], v[94:95], v[92:93], v[106:107] op_sel_hi:[0,1,1]
	s_waitcnt lgkmcnt(0)
	v_pk_fma_f32 v[118:119], v[94:95], v[96:97], v[108:109] op_sel_hi:[0,1,1]
	v_pk_fma_f32 v[126:127], v[114:115], v[96:97], v[102:103] op_sel_hi:[0,1,1]
	v_pk_fma_f32 v[96:97], v[114:115], v[98:99], v[104:105] op_sel_hi:[0,1,1]
	ds_read_b128 v[102:105], v167 offset:19456
	ds_read_b128 v[106:109], v167 offset:52224
	v_pk_fma_f32 v[112:113], v[94:95], v[90:91], v[124:125] op_sel_hi:[0,1,1]
	v_pk_fma_f32 v[120:121], v[94:95], v[98:99], v[120:121] op_sel_hi:[0,1,1]
	v_pk_fma_f32 v[124:125], v[114:115], v[92:93], v[100:101] op_sel_hi:[0,1,1]
	v_pk_fma_f32 v[110:111], v[114:115], v[90:91], v[110:111] op_sel_hi:[0,1,1]
	s_waitcnt lgkmcnt(1)
	v_pk_fma_f32 v[90:91], v[94:95], v[104:105], v[116:117] op_sel:[1,0,0]
	v_pk_fma_f32 v[98:99], v[94:95], v[102:103], v[112:113] op_sel:[1,0,0]
	s_waitcnt lgkmcnt(0)
	v_pk_fma_f32 v[92:93], v[94:95], v[108:109], v[120:121] op_sel:[1,0,0]
	v_pk_fma_f32 v[100:101], v[94:95], v[106:107], v[118:119] op_sel:[1,0,0]
	v_pk_fma_f32 v[94:95], v[114:115], v[104:105], v[124:125] op_sel:[1,0,0]
	v_pk_fma_f32 v[96:97], v[114:115], v[108:109], v[96:97] op_sel:[1,0,0]
	v_pk_fma_f32 v[104:105], v[114:115], v[106:107], v[126:127] op_sel:[1,0,0]
	ds_read_b128 v[106:109], v241 offset:5120
	v_pk_fma_f32 v[102:103], v[114:115], v[102:103], v[110:111] op_sel:[1,0,0]
	s_waitcnt lgkmcnt(0)
	v_pk_mul_f32 v[112:113], v[82:83], v[106:107]
	v_pk_mul_f32 v[82:83], v[86:87], v[138:139] op_sel_hi:[1,0]
	v_mov_b32_e32 v86, 0
	v_pk_mul_f32 v[106:107], v[82:83], v[106:107]
	v_med3_f32 v82, v112, s78, v179
	v_med3_f32 v83, v113, s78, v179
	v_cvt_pk_fp8_f32 v86, v82, v83
	v_pk_mul_f32 v[110:111], v[84:85], v[108:109]
	v_pk_mul_f32 v[84:85], v[88:89], v[138:139] op_sel_hi:[1,0]
	v_med3_f32 v82, v106, s78, v179
	v_pk_mul_f32 v[108:109], v[84:85], v[108:109]
	v_med3_f32 v84, v110, s78, v179
	v_med3_f32 v85, v111, s78, v179
	v_cvt_pk_fp8_f32 v86, v84, v85 op_sel:[0,0,1]
	v_med3_f32 v83, v107, s78, v179
	v_med3_f32 v84, v108, s78, v179
	v_med3_f32 v85, v109, s78, v179
	global_store_dword v[122:123], v86, off offset:-768
	v_mov_b32_e32 v86, 0
	v_cvt_pk_fp8_f32 v86, v82, v83
	v_cvt_pk_fp8_f32 v86, v84, v85 op_sel:[0,0,1]
	global_store_dword v[122:123], v86, off offset:1280
	ds_read_b128 v[82:85], v167 offset:20480
	ds_read_b128 v[86:89], v167 offset:53248
	s_waitcnt lgkmcnt(1)
	v_pk_fma_f32 v[98:99], v[112:113], v[82:83], v[98:99] op_sel_hi:[0,1,1]
	v_pk_fma_f32 v[90:91], v[112:113], v[84:85], v[90:91] op_sel_hi:[0,1,1]
	s_waitcnt lgkmcnt(0)
	v_pk_fma_f32 v[100:101], v[112:113], v[86:87], v[100:101] op_sel_hi:[0,1,1]
	v_pk_fma_f32 v[92:93], v[112:113], v[88:89], v[92:93] op_sel_hi:[0,1,1]
	v_pk_fma_f32 v[102:103], v[106:107], v[82:83], v[102:103] op_sel_hi:[0,1,1]
	v_pk_fma_f32 v[94:95], v[106:107], v[84:85], v[94:95] op_sel_hi:[0,1,1]
	v_pk_fma_f32 v[104:105], v[106:107], v[86:87], v[104:105] op_sel_hi:[0,1,1]
	v_pk_fma_f32 v[96:97], v[106:107], v[88:89], v[96:97] op_sel_hi:[0,1,1]
	ds_read_b128 v[82:85], v167 offset:21504
	ds_read_b128 v[86:89], v167 offset:54272
	s_waitcnt lgkmcnt(1)
	v_pk_fma_f32 v[90:91], v[112:113], v[84:85], v[90:91] op_sel:[1,0,0]
	v_pk_fma_f32 v[98:99], v[112:113], v[82:83], v[98:99] op_sel:[1,0,0]
	s_waitcnt lgkmcnt(0)
	v_pk_fma_f32 v[92:93], v[112:113], v[88:89], v[92:93] op_sel:[1,0,0]
	v_pk_fma_f32 v[100:101], v[112:113], v[86:87], v[100:101] op_sel:[1,0,0]
	v_pk_fma_f32 v[94:95], v[106:107], v[84:85], v[94:95] op_sel:[1,0,0]
	v_pk_fma_f32 v[102:103], v[106:107], v[82:83], v[102:103] op_sel:[1,0,0]
	v_pk_fma_f32 v[96:97], v[106:107], v[88:89], v[96:97] op_sel:[1,0,0]
	v_pk_fma_f32 v[104:105], v[106:107], v[86:87], v[104:105] op_sel:[1,0,0]
	ds_read_b128 v[82:85], v167 offset:22528
	ds_read_b128 v[86:89], v167 offset:55296
	s_waitcnt lgkmcnt(1)
	v_pk_fma_f32 v[98:99], v[110:111], v[82:83], v[98:99] op_sel_hi:[0,1,1]
	v_pk_fma_f32 v[90:91], v[110:111], v[84:85], v[90:91] op_sel_hi:[0,1,1]
	s_waitcnt lgkmcnt(0)
	v_pk_fma_f32 v[106:107], v[110:111], v[86:87], v[100:101] op_sel_hi:[0,1,1]
	v_pk_fma_f32 v[112:113], v[108:109], v[82:83], v[102:103] op_sel_hi:[0,1,1]
	v_pk_fma_f32 v[114:115], v[108:109], v[84:85], v[94:95] op_sel_hi:[0,1,1]
	ds_read_b128 v[82:85], v167 offset:23552
	ds_read_b128 v[100:103], v167 offset:56320
	v_pk_fma_f32 v[104:105], v[108:109], v[86:87], v[104:105] op_sel_hi:[0,1,1]
	v_pk_fma_f32 v[116:117], v[108:109], v[88:89], v[96:97] op_sel_hi:[0,1,1]
	v_pk_fma_f32 v[92:93], v[110:111], v[88:89], v[92:93] op_sel_hi:[0,1,1]
	s_waitcnt lgkmcnt(1)
	v_pk_fma_f32 v[86:87], v[110:111], v[84:85], v[90:91] op_sel:[1,0,0]
	v_pk_fma_f32 v[94:95], v[110:111], v[82:83], v[98:99] op_sel:[1,0,0]
	v_pk_fma_f32 v[90:91], v[108:109], v[84:85], v[114:115] op_sel:[1,0,0]
	v_pk_fma_f32 v[98:99], v[108:109], v[82:83], v[112:113] op_sel:[1,0,0]
	ds_read_b128 v[82:85], v241 offset:6144
	s_waitcnt lgkmcnt(0)
	v_pk_fma_f32 v[96:97], v[110:111], v[100:101], v[106:107] op_sel:[1,0,0]
	v_pk_fma_f32 v[100:101], v[108:109], v[100:101], v[104:105] op_sel:[1,0,0]
	v_pk_fma_f32 v[88:89], v[110:111], v[102:103], v[92:93] op_sel:[1,0,0]
	v_pk_fma_f32 v[92:93], v[108:109], v[102:103], v[116:117] op_sel:[1,0,0]
	s_waitcnt lgkmcnt(0)
	v_pk_mul_f32 v[104:105], v[74:75], v[82:83]
	v_pk_mul_f32 v[74:75], v[78:79], v[138:139] op_sel_hi:[1,0]
	v_mov_b32_e32 v78, 0
	v_pk_mul_f32 v[82:83], v[74:75], v[82:83]
	v_med3_f32 v74, v104, s78, v179
	v_med3_f32 v75, v105, s78, v179
	v_cvt_pk_fp8_f32 v78, v74, v75
	v_pk_mul_f32 v[102:103], v[76:77], v[84:85]
	v_pk_mul_f32 v[76:77], v[80:81], v[138:139] op_sel_hi:[1,0]
	v_med3_f32 v74, v82, s78, v179
	v_pk_mul_f32 v[106:107], v[76:77], v[84:85]
	v_med3_f32 v76, v102, s78, v179
	v_med3_f32 v77, v103, s78, v179
	v_cvt_pk_fp8_f32 v78, v76, v77 op_sel:[0,0,1]
	v_med3_f32 v75, v83, s78, v179
	v_med3_f32 v76, v106, s78, v179
	v_med3_f32 v77, v107, s78, v179
	global_store_dword v[122:123], v78, off offset:-512
	v_mov_b32_e32 v78, 0
	v_cvt_pk_fp8_f32 v78, v74, v75
	v_cvt_pk_fp8_f32 v78, v76, v77 op_sel:[0,0,1]
	global_store_dword v[122:123], v78, off offset:1536
	ds_read_b128 v[74:77], v167 offset:24576
	ds_read_b128 v[78:81], v167 offset:57344
	s_waitcnt lgkmcnt(1)
	v_pk_fma_f32 v[84:85], v[104:105], v[74:75], v[94:95] op_sel_hi:[0,1,1]
	v_pk_fma_f32 v[86:87], v[104:105], v[76:77], v[86:87] op_sel_hi:[0,1,1]
	s_waitcnt lgkmcnt(0)
	v_pk_fma_f32 v[94:95], v[104:105], v[78:79], v[96:97] op_sel_hi:[0,1,1]
	v_pk_fma_f32 v[88:89], v[104:105], v[80:81], v[88:89] op_sel_hi:[0,1,1]
	v_pk_fma_f32 v[96:97], v[82:83], v[74:75], v[98:99] op_sel_hi:[0,1,1]
	v_pk_fma_f32 v[90:91], v[82:83], v[76:77], v[90:91] op_sel_hi:[0,1,1]
	v_pk_fma_f32 v[98:99], v[82:83], v[78:79], v[100:101] op_sel_hi:[0,1,1]
	v_pk_fma_f32 v[92:93], v[82:83], v[80:81], v[92:93] op_sel_hi:[0,1,1]
	ds_read_b128 v[74:77], v167 offset:25600
	ds_read_b128 v[78:81], v167 offset:58368
	s_waitcnt lgkmcnt(1)
	v_pk_fma_f32 v[86:87], v[104:105], v[76:77], v[86:87] op_sel:[1,0,0]
	v_pk_fma_f32 v[84:85], v[104:105], v[74:75], v[84:85] op_sel:[1,0,0]
	s_waitcnt lgkmcnt(0)
	v_pk_fma_f32 v[88:89], v[104:105], v[80:81], v[88:89] op_sel:[1,0,0]
	v_pk_fma_f32 v[94:95], v[104:105], v[78:79], v[94:95] op_sel:[1,0,0]
	v_pk_fma_f32 v[90:91], v[82:83], v[76:77], v[90:91] op_sel:[1,0,0]
	v_pk_fma_f32 v[96:97], v[82:83], v[74:75], v[96:97] op_sel:[1,0,0]
	v_pk_fma_f32 v[92:93], v[82:83], v[80:81], v[92:93] op_sel:[1,0,0]
	v_pk_fma_f32 v[82:83], v[82:83], v[78:79], v[98:99] op_sel:[1,0,0]
	ds_read_b128 v[74:77], v167 offset:26624
	ds_read_b128 v[78:81], v167 offset:59392
	s_waitcnt lgkmcnt(1)
	v_pk_fma_f32 v[84:85], v[102:103], v[74:75], v[84:85] op_sel_hi:[0,1,1]
	v_pk_fma_f32 v[86:87], v[102:103], v[76:77], v[86:87] op_sel_hi:[0,1,1]
	s_waitcnt lgkmcnt(0)
	v_pk_fma_f32 v[94:95], v[102:103], v[78:79], v[94:95] op_sel_hi:[0,1,1]
	v_pk_fma_f32 v[88:89], v[102:103], v[80:81], v[88:89] op_sel_hi:[0,1,1]
	v_pk_fma_f32 v[96:97], v[106:107], v[74:75], v[96:97] op_sel_hi:[0,1,1]
	v_pk_fma_f32 v[98:99], v[106:107], v[76:77], v[90:91] op_sel_hi:[0,1,1]
	v_pk_fma_f32 v[100:101], v[106:107], v[78:79], v[82:83] op_sel_hi:[0,1,1]
	v_pk_fma_f32 v[104:105], v[106:107], v[80:81], v[92:93] op_sel_hi:[0,1,1]
	ds_read_b128 v[74:77], v167 offset:27648
	ds_read_b128 v[78:81], v167 offset:60416
	s_waitcnt lgkmcnt(1)
	v_pk_fma_f32 v[82:83], v[102:103], v[76:77], v[86:87] op_sel:[1,0,0]
	v_pk_fma_f32 v[90:91], v[102:103], v[74:75], v[84:85] op_sel:[1,0,0]
	s_waitcnt lgkmcnt(0)
	v_pk_fma_f32 v[92:93], v[102:103], v[78:79], v[94:95] op_sel:[1,0,0]
	v_pk_fma_f32 v[86:87], v[106:107], v[76:77], v[98:99] op_sel:[1,0,0]
	v_pk_fma_f32 v[94:95], v[106:107], v[74:75], v[96:97] op_sel:[1,0,0]
	ds_read_b128 v[74:77], v241 offset:7168
	v_pk_fma_f32 v[84:85], v[102:103], v[80:81], v[88:89] op_sel:[1,0,0]
	v_pk_fma_f32 v[88:89], v[106:107], v[80:81], v[104:105] op_sel:[1,0,0]
	v_pk_fma_f32 v[96:97], v[106:107], v[78:79], v[100:101] op_sel:[1,0,0]
	s_waitcnt lgkmcnt(0)
	v_pk_mul_f32 v[80:81], v[70:71], v[74:75]
	v_pk_mul_f32 v[74:75], v[66:67], v[74:75]
	v_med3_f32 v66, v80, s78, v179
	v_med3_f32 v67, v81, s78, v179
	v_mov_b32_e32 v70, 0
	v_cvt_pk_fp8_f32 v70, v66, v67
	v_pk_mul_f32 v[78:79], v[72:73], v[76:77]
	v_pk_mul_f32 v[76:77], v[68:69], v[76:77]
	v_med3_f32 v68, v78, s78, v179
	v_med3_f32 v69, v79, s78, v179
	v_cvt_pk_fp8_f32 v70, v68, v69 op_sel:[0,0,1]
	v_med3_f32 v66, v74, s78, v179
	v_med3_f32 v67, v75, s78, v179
	v_med3_f32 v68, v76, s78, v179
	global_store_dword v[122:123], v70, off offset:-256
	v_mov_b32_e32 v70, 0
	v_cvt_pk_fp8_f32 v70, v66, v67
	v_med3_f32 v69, v77, s78, v179
	v_cvt_pk_fp8_f32 v70, v68, v69 op_sel:[0,0,1]
	global_store_dword v[122:123], v70, off offset:1792
	ds_read_b128 v[66:69], v167 offset:28672
	ds_read_b128 v[70:73], v167 offset:61440
	s_waitcnt lgkmcnt(1)
	v_pk_fma_f32 v[90:91], v[80:81], v[66:67], v[90:91] op_sel_hi:[0,1,1]
	v_pk_fma_f32 v[98:99], v[80:81], v[68:69], v[82:83] op_sel_hi:[0,1,1]
	s_waitcnt lgkmcnt(0)
	v_pk_fma_f32 v[82:83], v[80:81], v[70:71], v[92:93] op_sel_hi:[0,1,1]
	v_pk_fma_f32 v[92:93], v[80:81], v[72:73], v[84:85] op_sel_hi:[0,1,1]
	v_pk_fma_f32 v[84:85], v[74:75], v[66:67], v[94:95] op_sel_hi:[0,1,1]
	v_pk_fma_f32 v[94:95], v[74:75], v[68:69], v[86:87] op_sel_hi:[0,1,1]
	v_pk_fma_f32 v[86:87], v[74:75], v[70:71], v[96:97] op_sel_hi:[0,1,1]
	v_pk_fma_f32 v[88:89], v[74:75], v[72:73], v[88:89] op_sel_hi:[0,1,1]
	ds_read_b128 v[66:69], v167 offset:29696
	ds_read_b128 v[70:73], v167 offset:62464
	s_waitcnt lgkmcnt(1)
	v_pk_fma_f32 v[96:97], v[80:81], v[68:69], v[98:99] op_sel:[1,0,0]
	v_pk_fma_f32 v[90:91], v[80:81], v[66:67], v[90:91] op_sel:[1,0,0]
	s_waitcnt lgkmcnt(0)
	v_pk_fma_f32 v[92:93], v[80:81], v[72:73], v[92:93] op_sel:[1,0,0]
	v_pk_fma_f32 v[80:81], v[80:81], v[70:71], v[82:83] op_sel:[1,0,0]
	v_pk_fma_f32 v[82:83], v[74:75], v[68:69], v[94:95] op_sel:[1,0,0]
	v_pk_fma_f32 v[84:85], v[74:75], v[66:67], v[84:85] op_sel:[1,0,0]
	v_pk_fma_f32 v[88:89], v[74:75], v[72:73], v[88:89] op_sel:[1,0,0]
	v_pk_fma_f32 v[74:75], v[74:75], v[70:71], v[86:87] op_sel:[1,0,0]
	ds_read_b128 v[66:69], v167 offset:30720
	ds_read_b128 v[70:73], v167 offset:63488
	s_waitcnt lgkmcnt(1)
	v_pk_fma_f32 v[86:87], v[78:79], v[66:67], v[90:91] op_sel_hi:[0,1,1]
	v_pk_fma_f32 v[90:91], v[78:79], v[68:69], v[96:97] op_sel_hi:[0,1,1]
	s_waitcnt lgkmcnt(0)
	v_pk_fma_f32 v[80:81], v[78:79], v[70:71], v[80:81] op_sel_hi:[0,1,1]
	v_pk_fma_f32 v[92:93], v[78:79], v[72:73], v[92:93] op_sel_hi:[0,1,1]
	v_pk_fma_f32 v[84:85], v[76:77], v[66:67], v[84:85] op_sel_hi:[0,1,1]
	v_pk_fma_f32 v[82:83], v[76:77], v[68:69], v[82:83] op_sel_hi:[0,1,1]
	v_pk_fma_f32 v[74:75], v[76:77], v[70:71], v[74:75] op_sel_hi:[0,1,1]
	v_pk_fma_f32 v[88:89], v[76:77], v[72:73], v[88:89] op_sel_hi:[0,1,1]
	ds_read_b128 v[66:69], v167 offset:31744
	ds_read_b128 v[70:73], v167 offset:64512
	s_waitcnt lgkmcnt(1)
	v_pk_fma_f32 v[86:87], v[78:79], v[66:67], v[86:87] op_sel:[1,0,0]
	v_pk_fma_f32 v[90:91], v[78:79], v[68:69], v[90:91] op_sel:[1,0,0]
	s_waitcnt lgkmcnt(0)
	v_pk_fma_f32 v[92:93], v[78:79], v[72:73], v[92:93] op_sel:[1,0,0]
	v_pk_fma_f32 v[78:79], v[78:79], v[70:71], v[80:81] op_sel:[1,0,0]
	v_pk_fma_f32 v[70:71], v[76:77], v[70:71], v[74:75] op_sel:[1,0,0]
	v_cndmask_b32_e64 v75, v86, v87, s[6:7]
	v_pk_fma_f32 v[68:69], v[76:77], v[68:69], v[82:83] op_sel:[1,0,0]
	v_pk_fma_f32 v[66:67], v[76:77], v[66:67], v[84:85] op_sel:[1,0,0]
	v_pk_fma_f32 v[72:73], v[76:77], v[72:73], v[88:89] op_sel:[1,0,0]
	ds_bpermute_b32 v75, v1, v75
	v_cndmask_b32_e64 v76, v90, v91, s[6:7]
	ds_bpermute_b32 v76, v1, v76
	v_cndmask_b32_e64 v74, v87, v86, s[6:7]
	v_cndmask_b32_e64 v77, v78, v79, s[6:7]
	s_waitcnt lgkmcnt(1)
	v_add_f32_e32 v74, v74, v75
	v_cndmask_b32_e64 v75, v91, v90, s[6:7]
	s_waitcnt lgkmcnt(0)
	v_add_f32_e32 v75, v75, v76
	v_cndmask_b32_e64 v76, v79, v78, s[6:7]
	ds_bpermute_b32 v77, v1, v77
	v_cndmask_b32_e64 v78, v92, v93, s[6:7]
	ds_bpermute_b32 v78, v1, v78
	s_waitcnt lgkmcnt(1)
	v_add_f32_e32 v76, v76, v77
	v_cndmask_b32_e64 v77, v93, v92, s[6:7]
	s_waitcnt lgkmcnt(0)
	v_add_f32_e32 v77, v77, v78
	v_cndmask_b32_e64 v78, v67, v66, s[6:7]
	v_cndmask_b32_e64 v66, v66, v67, s[6:7]
	v_cndmask_b32_e64 v67, v69, v68, s[6:7]
	v_cndmask_b32_e64 v68, v68, v69, s[6:7]
	ds_bpermute_b32 v68, v1, v68
	v_cndmask_b32_e64 v69, v70, v71, s[6:7]
	ds_bpermute_b32 v69, v1, v69
	ds_bpermute_b32 v66, v1, v66
	s_waitcnt lgkmcnt(2)
	v_add_f32_e32 v67, v67, v68
	v_cndmask_b32_e64 v68, v71, v70, s[6:7]
	v_cndmask_b32_e64 v70, v72, v73, s[6:7]
	ds_bpermute_b32 v70, v1, v70
	v_cndmask_b32_e64 v71, v74, v75, s[8:9]
	s_waitcnt lgkmcnt(2)
	v_add_f32_e32 v68, v68, v69
	v_cndmask_b32_e64 v69, v73, v72, s[6:7]
	ds_bpermute_b32 v71, v135, v71
	v_cndmask_b32_e64 v72, v76, v77, s[8:9]
	ds_bpermute_b32 v72, v135, v72
	s_waitcnt lgkmcnt(2)
	v_add_f32_e32 v69, v69, v70
	v_cndmask_b32_e64 v70, v75, v74, s[8:9]
	v_add_f32_e32 v66, v78, v66
	s_waitcnt lgkmcnt(1)
	v_add_f32_e32 v70, v70, v71
	v_cndmask_b32_e64 v71, v77, v76, s[8:9]
	s_waitcnt lgkmcnt(0)
	v_add_f32_e32 v71, v71, v72
	v_cndmask_b32_e64 v72, v67, v66, s[8:9]
	v_cndmask_b32_e64 v66, v66, v67, s[8:9]
	v_cndmask_b32_e64 v67, v69, v68, s[8:9]
	v_cndmask_b32_e64 v68, v68, v69, s[8:9]
	ds_bpermute_b32 v66, v135, v66
	ds_bpermute_b32 v68, v135, v68
	v_cndmask_b32_e64 v69, v70, v71, s[10:11]
	ds_bpermute_b32 v69, v137, v69
	s_waitcnt lgkmcnt(2)
	v_add_f32_e32 v66, v72, v66
	s_waitcnt lgkmcnt(1)
	v_add_f32_e32 v67, v67, v68
	v_cndmask_b32_e64 v68, v71, v70, s[10:11]
	s_waitcnt lgkmcnt(0)
	v_add_f32_e32 v68, v68, v69
	v_cndmask_b32_e64 v69, v67, v66, s[10:11]
	v_cndmask_b32_e64 v66, v66, v67, s[10:11]
	ds_bpermute_b32 v66, v137, v66
	s_waitcnt lgkmcnt(0)
	v_add_f32_e32 v66, v69, v66
	v_cndmask_b32_e64 v67, v66, v68, s[12:13]
	v_cndmask_b32_e64 v66, v68, v66, s[12:13]
	ds_bpermute_b32 v66, v147, v66
	s_waitcnt lgkmcnt(0)
	v_add_f32_e32 v66, v67, v66
	ds_bpermute_b32 v67, v164, v66
	s_waitcnt lgkmcnt(0)
	v_add_f32_e32 v66, v66, v67
	ds_bpermute_b32 v67, v165, v66
	s_waitcnt lgkmcnt(0)
	v_add_f32_e32 v66, v66, v67
	s_nop 0
	v_readlane_b32 s74, v66, 0
	v_readlane_b32 s73, v66, 1
	v_readlane_b32 s72, v66, 2
	v_readlane_b32 s27, v66, 3
	v_readlane_b32 s26, v66, 4
	v_readlane_b32 s25, v66, 5
	v_readlane_b32 s24, v66, 6
	v_readlane_b32 s71, v66, 7
	v_readlane_b32 s86, v66, 8
	v_readlane_b32 s85, v66, 9
	v_readlane_b32 s84, v66, 10
	v_readlane_b32 s83, v66, 11
	v_readlane_b32 s82, v66, 12
	v_readlane_b32 s81, v66, 13
	v_readlane_b32 s80, v66, 14
	v_readlane_b32 s75, v66, 15
	s_and_saveexec_b64 s[68:69], s[4:5]
	s_cbranch_execz .LBB0_917
	v_mov_b32_e32 v66, s74
	v_cmp_gt_f32_e64 s[0:1], s73, v66
	v_mov_b32_e32 v67, s73
	v_mov_b32_e32 v69, s72
	v_cndmask_b32_e64 v68, v66, v67, s[0:1]
	v_cmp_gt_f32_e64 s[14:15], s72, v68
	v_mov_b32_e32 v70, s27
	v_mov_b32_e32 v71, s26
	v_cndmask_b32_e64 v68, v68, v69, s[14:15]
	v_cmp_gt_f32_e64 s[16:17], s27, v68
	v_mov_b32_e32 v72, s25
	v_mov_b32_e32 v73, s24
	v_cndmask_b32_e64 v68, v68, v70, s[16:17]
	v_cmp_gt_f32_e64 s[18:19], s26, v68
	s_add_i32 s79, s77, s37
	s_add_i32 s79, s79, 0x10000
	v_cndmask_b32_e64 v68, v68, v71, s[18:19]
	v_cmp_gt_f32_e64 s[20:21], s25, v68
	v_cndmask_b32_e64 v74, 0, 1, s[0:1]
	v_mov_b32_e32 v75, s80
	v_cndmask_b32_e64 v68, v68, v72, s[20:21]
	v_cmp_gt_f32_e64 s[22:23], s24, v68
	s_nop 1
	v_cndmask_b32_e64 v68, v68, v73, s[22:23]
	v_cmp_ngt_f32_e32 vcc, s71, v68
	s_and_b64 s[90:91], s[22:23], vcc
	s_and_b64 s[0:1], s[14:15], exec
	v_readfirstlane_b32 s0, v74
	s_cselect_b32 s14, 2, s0
	s_and_b64 s[0:1], s[16:17], exec
	s_cselect_b32 s14, 3, s14
	s_and_b64 s[0:1], s[18:19], exec
	s_cselect_b32 s14, 4, s14
	s_and_b64 s[0:1], s[20:21], exec
	s_cselect_b32 s14, 5, s14
	s_and_b64 s[0:1], s[22:23], exec
	s_cselect_b32 s14, 6, s14
	s_and_b64 s[0:1], vcc, exec
	s_cselect_b32 s70, s14, 7
	s_cmp_lg_u32 s70, 5
	s_cselect_b64 s[92:93], -1, 0
	s_cmp_lg_u32 s70, 4
	s_cselect_b64 s[22:23], -1, 0
	s_cmp_lg_u32 s70, 3
	s_cselect_b64 s[20:21], -1, 0
	s_cmp_lg_u32 s70, 2
	s_cselect_b64 s[18:19], -1, 0
	s_cmp_lg_u32 s70, 1
	s_cselect_b64 s[16:17], -1, 0
	s_cmp_eq_u32 s70, 0
	s_cselect_b64 s[14:15], -1, 0
	v_cmp_nlg_f32_e64 s[0:1], s74, v180
	s_or_b64 s[0:1], s[14:15], s[0:1]
	v_mov_b32_e32 v74, s81
	v_cndmask_b32_e64 v66, v66, v180, s[0:1]
	v_cmp_gt_f32_e64 s[14:15], s73, v66
	s_and_b64 s[14:15], s[16:17], s[14:15]
	s_nop 0
	v_cndmask_b32_e64 v66, v66, v67, s[14:15]
	v_cmp_gt_f32_e64 s[16:17], s72, v66
	s_and_b64 s[16:17], s[18:19], s[16:17]
	v_mov_b32_e32 v67, s71
	v_cndmask_b32_e64 v66, v66, v69, s[16:17]
	v_cmp_gt_f32_e64 s[18:19], s27, v66
	s_and_b64 s[18:19], s[20:21], s[18:19]
	v_cndmask_b32_e64 v69, 0, -1, s[0:1]
	v_cndmask_b32_e64 v66, v66, v70, s[18:19]
	v_cmp_gt_f32_e64 s[20:21], s26, v66
	s_and_b64 s[20:21], s[22:23], s[20:21]
	s_nop 0
	v_cndmask_b32_e64 v66, v66, v71, s[20:21]
	v_cmp_gt_f32_e64 s[22:23], s25, v66
	s_and_b64 s[22:23], s[92:93], s[22:23]
	s_nop 0
	v_cndmask_b32_e64 v66, v66, v72, s[22:23]
	v_cmp_ngt_f32_e64 s[24:25], s24, v66
	s_or_b64 s[24:25], s[90:91], s[24:25]
	s_nop 0
	v_cndmask_b32_e64 v66, v73, v66, s[24:25]
	v_cmp_gt_f32_e64 s[26:27], s71, v66
	s_and_b64 s[26:27], vcc, s[26:27]
	v_mov_b32_e32 v73, s82
	v_cndmask_b32_e64 v66, v66, v67, s[26:27]
	v_cndmask_b32_e32 v67, v67, v68, vcc
	v_sub_f32_e32 v66, v66, v67
	v_mul_f32_e32 v66, 0x3fb8aa3b, v66
	v_exp_f32_e32 v66, v66
	s_nop 0
	v_add_f32_e32 v66, 1.0, v66
	v_div_scale_f32 v67, s[0:1], v66, v66, 1.0
	v_rcp_f32_e32 v68, v67
	v_readfirstlane_b32 s0, v69
	s_lshl_b32 s71, s0, 8
	s_and_b64 s[0:1], s[14:15], exec
	v_fma_f32 v70, -v67, v68, 1.0
	s_cselect_b32 s14, 0x100, s71
	s_and_b64 s[0:1], s[16:17], exec
	v_fmac_f32_e32 v68, v70, v68
	v_div_scale_f32 v70, vcc, 1.0, v66, 1.0
	s_cselect_b32 s14, 0x200, s14
	s_and_b64 s[0:1], s[18:19], exec
	v_mul_f32_e32 v71, v70, v68
	s_cselect_b32 s14, 0x300, s14
	s_and_b64 s[0:1], s[20:21], exec
	v_fma_f32 v72, -v67, v71, v70
	s_cselect_b32 s14, 0x400, s14
	s_and_b64 s[0:1], s[22:23], exec
	v_fmac_f32_e32 v71, v72, v68
	s_cselect_b32 s14, 0x500, s14
	s_and_b64 s[0:1], s[24:25], exec
	v_fma_f32 v67, -v67, v71, v70
	s_cselect_b32 s14, s14, 0x600
	s_and_b64 s[0:1], s[26:27], exec
	v_div_fmas_f32 v67, v67, v68, v71
	s_cselect_b32 s0, 0x700, s14
	v_mov_b32_e32 v68, s86
	s_add_i32 s74, s0, s70
	v_cmp_gt_f32_e64 s[0:1], s85, v68
	v_mov_b32_e32 v69, s85
	v_mov_b32_e32 v71, s84
	v_cndmask_b32_e64 v70, v68, v69, s[0:1]
	v_cmp_gt_f32_e64 s[14:15], s84, v70
	v_mov_b32_e32 v72, s83
	s_add_u32 s72, s46, s66
	v_cndmask_b32_e64 v70, v70, v71, s[14:15]
	v_cmp_gt_f32_e64 s[16:17], s83, v70
	s_addc_u32 s73, s47, s67
	s_add_u32 s70, s46, s64
	v_cndmask_b32_e64 v70, v70, v72, s[16:17]
	v_cmp_gt_f32_e64 s[18:19], s82, v70
	s_addc_u32 s71, s47, s65
	v_cndmask_b32_e64 v76, 0, 1, s[0:1]
	v_cndmask_b32_e64 v70, v70, v73, s[18:19]
	v_cmp_gt_f32_e64 s[20:21], s81, v70
	v_div_fixup_f32 v66, v67, v66, 1.0
	v_sub_f32_e32 v67, 1.0, v66
	v_cndmask_b32_e64 v70, v70, v74, s[20:21]
	v_cmp_gt_f32_e64 s[22:23], s80, v70
	s_nop 1
	v_cndmask_b32_e64 v70, v70, v75, s[22:23]
	v_cmp_ngt_f32_e32 vcc, s75, v70
	s_and_b64 s[26:27], s[22:23], vcc
	s_and_b64 s[0:1], s[14:15], exec
	v_readfirstlane_b32 s0, v76
	s_cselect_b32 s14, 2, s0
	s_and_b64 s[0:1], s[16:17], exec
	s_cselect_b32 s14, 3, s14
	s_and_b64 s[0:1], s[18:19], exec
	s_cselect_b32 s14, 4, s14
	s_and_b64 s[0:1], s[20:21], exec
	s_cselect_b32 s14, 5, s14
	s_and_b64 s[0:1], s[22:23], exec
	s_cselect_b32 s14, 6, s14
	s_and_b64 s[0:1], vcc, exec
	s_cselect_b32 s87, s14, 7
	s_cmp_lg_u32 s87, 5
	s_cselect_b64 s[24:25], -1, 0
	s_cmp_lg_u32 s87, 4
	s_cselect_b64 s[22:23], -1, 0
	s_cmp_lg_u32 s87, 3
	s_cselect_b64 s[20:21], -1, 0
	s_cmp_lg_u32 s87, 2
	s_cselect_b64 s[18:19], -1, 0
	s_cmp_lg_u32 s87, 1
	s_cselect_b64 s[16:17], -1, 0
	s_cmp_eq_u32 s87, 0
	s_cselect_b64 s[14:15], -1, 0
	v_cmp_nlg_f32_e64 s[0:1], s86, v180
	s_or_b64 s[0:1], s[14:15], s[0:1]
	s_nop 0
	v_cndmask_b32_e64 v68, v68, v180, s[0:1]
	v_cmp_gt_f32_e64 s[14:15], s85, v68
	s_and_b64 s[14:15], s[16:17], s[14:15]
	s_nop 0
	v_cndmask_b32_e64 v68, v68, v69, s[14:15]
	v_cmp_gt_f32_e64 s[16:17], s84, v68
	s_and_b64 s[16:17], s[18:19], s[16:17]
	v_mov_b32_e32 v69, s75
	v_cndmask_b32_e64 v68, v68, v71, s[16:17]
	v_cmp_gt_f32_e64 s[18:19], s83, v68
	s_and_b64 s[18:19], s[20:21], s[18:19]
	v_cndmask_b32_e64 v71, 0, -1, s[0:1]
	v_cndmask_b32_e64 v68, v68, v72, s[18:19]
	v_cmp_gt_f32_e64 s[20:21], s82, v68
	s_and_b64 s[20:21], s[22:23], s[20:21]
	s_nop 0
	v_cndmask_b32_e64 v68, v68, v73, s[20:21]
	v_cmp_gt_f32_e64 s[22:23], s81, v68
	s_and_b64 s[22:23], s[24:25], s[22:23]
	s_nop 0
	v_cndmask_b32_e64 v68, v68, v74, s[22:23]
	v_cmp_ngt_f32_e64 s[24:25], s80, v68
	s_or_b64 s[24:25], s[26:27], s[24:25]
	s_nop 0
	v_cndmask_b32_e64 v68, v75, v68, s[24:25]
	v_cmp_gt_f32_e64 s[26:27], s75, v68
	s_and_b64 s[26:27], vcc, s[26:27]
	s_nop 0
	v_cndmask_b32_e64 v68, v68, v69, s[26:27]
	v_cndmask_b32_e32 v69, v69, v70, vcc
	v_sub_f32_e32 v68, v68, v69
	v_mul_f32_e32 v68, 0x3fb8aa3b, v68
	v_exp_f32_e32 v68, v68
	s_nop 0
	v_add_f32_e32 v68, 1.0, v68
	v_div_scale_f32 v69, s[0:1], v68, v68, 1.0
	v_rcp_f32_e32 v70, v69
	v_readfirstlane_b32 s0, v71
	s_lshl_b32 s75, s0, 8
	s_and_b64 s[0:1], s[14:15], exec
	v_fma_f32 v72, -v69, v70, 1.0
	v_fmac_f32_e32 v70, v72, v70
	v_div_scale_f32 v72, vcc, 1.0, v68, 1.0
	s_cselect_b32 s14, 0x100, s75
	s_and_b64 s[0:1], s[16:17], exec
	v_mul_f32_e32 v73, v72, v70
	s_cselect_b32 s14, 0x200, s14
	s_and_b64 s[0:1], s[18:19], exec
	v_fma_f32 v74, -v69, v73, v72
	s_cselect_b32 s14, 0x300, s14
	s_and_b64 s[0:1], s[20:21], exec
	v_fmac_f32_e32 v73, v74, v70
	s_cselect_b32 s14, 0x400, s14
	s_and_b64 s[0:1], s[22:23], exec
	v_fma_f32 v69, -v69, v73, v72
	s_cselect_b32 s14, 0x500, s14
	s_and_b64 s[0:1], s[24:25], exec
	v_div_fmas_f32 v69, v69, v70, v73
	s_cselect_b32 s14, s14, 0x600
	s_and_b64 s[0:1], s[26:27], exec
	v_div_fixup_f32 v68, v69, v68, 1.0
	s_cselect_b32 s0, 0x700, s14
	s_add_i32 s75, s0, s87
	v_sub_f32_e32 v69, 1.0, v68
	v_mov_b64_e32 v[70:71], s[74:75]
	global_store_dwordx4 v139, v[66:69], s[70:71] offset:-8
	global_store_dwordx2 v177, v[70:71], s[72:73]
	s_nop 0
	v_mov_b32_e32 v66, s79
	ds_write_b64 v66, v[70:71]
	s_branch .LBB0_917
